# SwiGLU epilogue: scalar mul(-log2e)/add(1.0) pairs -> v_pk_mul_f32/v_pk_add_f32 (same f32 ops), constants in dead fragment regs
# speedup vs baseline: 1.0034x; 1.0034x over previous
; __device__ __forceinline__ unsigned cvt_pk_bf16(float lo, float hi) { const f32x2_t v = {lo, hi}; const bf16x2_t b = __builtin_convertvector(v, bf16x2_t); return __builtin_bit_cast(unsigned, b); }
;     __device__ __forceinline__ void operator()(const f32x4 (&acc)[2][2][4][2], const Unit& u, int wr, int wc, int fr, int fq, int ui) const {
;     ...
;         for (int ai = 0; ai < 2; ++ai)
; #pragma unroll
;             for (int m = 0; m < 4; ++m) rs[ai][m] = rtab[ui * 256 + ai * HALF + wr * 64 + m * 16 + fr];
; #pragma unroll
;         for (int ai = 0; ai < 2; ++ai)
; #pragma unroll
;             for (int m = 0; m < 4; ++m) {
;                 const float r = rs[ai][m]; const int row = u.pm * BM + ai * HALF + wr * 64 + m * 16 + fr;
;                 float g[8], v[8], e[8];
; #pragma unroll
;                 for (int n = 0; n < 2; ++n)
; #pragma unroll
;                     for (int i = 0; i < 4; ++i) { g[n * 4 + i] = fmaf(acc[ai][0][m][n][i], r, bg[n][i]); v[n * 4 + i] = fmaf(acc[ai][1][m][n][i], r, bu[n][i]); }
; #pragma unroll
;                 for (int i = 0; i < 8; ++i) e[i] = __builtin_amdgcn_exp2f(g[i] * (-LOG2E));
; #pragma unroll
;                 for (int i = 0; i < 8; ++i) e[i] = __builtin_amdgcn_rcpf(1.0f + e[i]);
; #pragma unroll
;                 for (int i = 0; i < 8; ++i) e[i] = (g[i] * e[i]) * v[i];
;                 u32x4 w; w.x = cvt_pk_bf16(e[0], e[1]); w.y = cvt_pk_bf16(e[2], e[3]); w.z = cvt_pk_bf16(e[4], e[5]); w.w = cvt_pk_bf16(e[6], e[7]);
;                 *(u32x4*)(act + ((size_t)((row >> 8) * (F / 64) + (jcol >> 6)) * 256 + (row & 255)) * 64 + (jcol & 63)) = w;
.LBB0_249:
	v_lshl_add_u32 v162, s56, 8, v171
	v_lshl_add_u32 v162, v162, 2, 0
	v_lshl_add_u32 v84, s56, 10, v179
	v_add_u32_e32 v162, 0x22000, v162
	ds_read_b128 v[96:99], v84
	ds_read_b128 v[80:83], v84 offset:16
	ds_read_b128 v[100:103], v84 offset:512
	ds_read_b128 v[84:87], v84 offset:528
	ds_read2_b32 v[166:167], v162 offset1:16
	ds_read2_b32 v[176:177], v162 offset0:32 offset1:48
	ds_read2_b32 v[164:165], v162 offset0:128 offset1:144
	ds_read2_b32 v[162:163], v162 offset0:160 offset1:176
	s_lshl_b32 s11, s55, 8
	s_waitcnt lgkmcnt(0)
	v_mov_b32_e32 v222, 0xbfb8aa3b
	v_mov_b32_e32 v224, 1.0
	v_pk_fma_f32 v[142:143], v[142:143], v[166:167], v[96:97] op_sel_hi:[1,0,1]
	v_pk_fma_f32 v[138:139], v[138:139], v[166:167], v[100:101] op_sel_hi:[1,0,1]
	v_pk_mul_f32 v[168:169], v[142:143], v[222:223] op_sel_hi:[1,0]
	v_exp_f32_e32 v168, v168
	v_exp_f32_e32 v169, v169
	v_pk_fma_f32 v[140:141], v[140:141], v[166:167], v[102:103] op_sel_hi:[1,0,1]
	v_pk_fma_f32 v[134:135], v[134:135], v[166:167], v[80:81] op_sel_hi:[1,0,1]
	v_pk_add_f32 v[168:169], v[168:169], v[224:225] op_sel_hi:[1,0]
	v_rcp_f32_e32 v168, v168
	v_rcp_f32_e32 v169, v169
	v_pk_fma_f32 v[130:131], v[130:131], v[166:167], v[84:85] op_sel_hi:[1,0,1]
	s_lshl_b32 s9, s57, 7
	s_add_i32 s16, s11, s49
	v_pk_mul_f32 v[142:143], v[142:143], v[168:169]
	s_or_b32 s9, s9, s50
	v_pk_mul_f32 v[138:139], v[138:139], v[142:143]
	v_pk_fma_f32 v[142:143], v[144:145], v[166:167], v[98:99] op_sel_hi:[1,0,1]
	s_ashr_i32 s16, s16, 8
	v_pk_mul_f32 v[144:145], v[142:143], v[222:223] op_sel_hi:[1,0]
	v_exp_f32_e32 v144, v144
	v_exp_f32_e32 v145, v145
	s_ashr_i32 s9, s9, 6
	s_mulk_i32 s16, 0x58
	v_pk_add_f32 v[144:145], v[144:145], v[224:225] op_sel_hi:[1,0]
	v_rcp_f32_e32 v144, v144
	v_rcp_f32_e32 v145, v145
	s_add_i32 s16, s16, s9
	s_ashr_i32 s17, s16, 31
	v_pk_fma_f32 v[132:133], v[132:133], v[166:167], v[86:87] op_sel_hi:[1,0,1]
	v_pk_mul_f32 v[142:143], v[142:143], v[144:145]
	s_lshl_b64 s[16:17], s[16:17], 15
	v_pk_mul_f32 v[140:141], v[140:141], v[142:143]
	v_pk_mul_f32 v[142:143], v[134:135], v[222:223] op_sel_hi:[1,0]
	v_exp_f32_e32 v142, v142
	v_exp_f32_e32 v143, v143
	v_pk_fma_f32 v[108:109], v[108:109], v[176:177], v[96:97] op_sel_hi:[1,0,1]
	v_pk_fma_f32 v[104:105], v[104:105], v[176:177], v[100:101] op_sel_hi:[1,0,1]
	v_pk_add_f32 v[142:143], v[142:143], v[224:225] op_sel_hi:[1,0]
	v_rcp_f32_e32 v142, v142
	v_rcp_f32_e32 v143, v143
	v_pk_fma_f32 v[106:107], v[106:107], v[176:177], v[102:103] op_sel_hi:[1,0,1]
	v_pk_fma_f32 v[92:93], v[92:93], v[176:177], v[80:81] op_sel_hi:[1,0,1]
	v_pk_fma_f32 v[88:89], v[88:89], v[176:177], v[84:85] op_sel_hi:[1,0,1]
	v_pk_mul_f32 v[134:135], v[134:135], v[142:143]
	v_pk_fma_f32 v[90:91], v[90:91], v[176:177], v[86:87] op_sel_hi:[1,0,1]
	v_pk_mul_f32 v[130:131], v[130:131], v[134:135]
	v_pk_fma_f32 v[134:135], v[136:137], v[166:167], v[82:83] op_sel_hi:[1,0,1]
	s_movk_i32 s18, 0x1000
	v_pk_mul_f32 v[136:137], v[134:135], v[222:223] op_sel_hi:[1,0]
	v_exp_f32_e32 v136, v136
	v_exp_f32_e32 v137, v137
	v_pk_fma_f32 v[60:61], v[60:61], v[164:165], v[96:97] op_sel_hi:[1,0,1]
	v_pk_fma_f32 v[56:57], v[56:57], v[164:165], v[100:101] op_sel_hi:[1,0,1]
	v_pk_add_f32 v[136:137], v[136:137], v[224:225] op_sel_hi:[1,0]
	v_rcp_f32_e32 v136, v136
	v_rcp_f32_e32 v137, v137
	v_pk_fma_f32 v[58:59], v[58:59], v[164:165], v[102:103] op_sel_hi:[1,0,1]
	v_pk_fma_f32 v[52:53], v[52:53], v[164:165], v[80:81] op_sel_hi:[1,0,1]
	v_pk_fma_f32 v[48:49], v[48:49], v[164:165], v[84:85] op_sel_hi:[1,0,1]
	v_pk_mul_f32 v[134:135], v[134:135], v[136:137]
	s_add_i32 s11, s11, s53
	v_pk_mul_f32 v[136:137], v[132:133], v[134:135]
	v_cvt_pk_bf16_f32 v134, v130, v131
	v_lshl_add_u64 v[130:131], v[154:155], 0, s[16:17]
	v_cvt_pk_bf16_f32 v132, v138, v139
	v_cvt_pk_bf16_f32 v133, v140, v141
	v_cvt_pk_bf16_f32 v135, v136, v137
	v_lshl_add_u64 v[130:131], v[130:131], 0, v[128:129]
	global_store_dwordx4 v[130:131], v[132:135], off
	s_ashr_i32 s11, s11, 8
	s_mulk_i32 s11, 0x58
	v_mov_b32_e32 v132, v167
	v_pk_fma_f32 v[124:125], v[124:125], v[132:133], v[96:97] op_sel_hi:[1,0,1]
	v_pk_fma_f32 v[120:121], v[120:121], v[132:133], v[100:101] op_sel_hi:[1,0,1]
	v_mul_f32_e32 v133, 0xbfb8aa3b, v124
	v_exp_f32_e32 v133, v133
	v_mul_f32_e32 v134, 0xbfb8aa3b, v125
	v_exp_f32_e32 v135, v134
	s_add_i32 s16, s11, s9
	v_add_f32_e32 v133, 1.0, v133
	v_rcp_f32_e32 v134, v133
	v_add_f32_e32 v133, 1.0, v135
	v_rcp_f32_e32 v135, v133
	v_pk_fma_f32 v[122:123], v[122:123], v[132:133], v[102:103] op_sel_hi:[1,0,1]
	v_pk_fma_f32 v[116:117], v[116:117], v[132:133], v[80:81] op_sel_hi:[1,0,1]
	v_pk_fma_f32 v[112:113], v[112:113], v[132:133], v[84:85] op_sel_hi:[1,0,1]
	v_pk_mul_f32 v[124:125], v[124:125], v[134:135]
	v_pk_fma_f32 v[114:115], v[114:115], v[132:133], v[86:87] op_sel_hi:[1,0,1]
	v_pk_mul_f32 v[120:121], v[120:121], v[124:125]
	v_pk_fma_f32 v[124:125], v[126:127], v[132:133], v[98:99] op_sel_hi:[1,0,1]
	s_ashr_i32 s17, s16, 31
	v_pk_mul_f32 v[126:127], v[124:125], v[222:223] op_sel_hi:[1,0]
	v_exp_f32_e32 v126, v126
	v_exp_f32_e32 v127, v127
	v_pk_fma_f32 v[50:51], v[50:51], v[164:165], v[86:87] op_sel_hi:[1,0,1]
	s_lshl_b64 s[16:17], s[16:17], 15
	v_pk_add_f32 v[126:127], v[126:127], v[224:225] op_sel_hi:[1,0]
	v_rcp_f32_e32 v126, v126
	v_rcp_f32_e32 v127, v127
	v_pk_fma_f32 v[28:29], v[28:29], v[162:163], v[96:97] op_sel_hi:[1,0,1]
	v_pk_fma_f32 v[24:25], v[24:25], v[162:163], v[100:101] op_sel_hi:[1,0,1]
	v_pk_fma_f32 v[26:27], v[26:27], v[162:163], v[102:103] op_sel_hi:[1,0,1]
	v_pk_mul_f32 v[124:125], v[124:125], v[126:127]
	v_pk_fma_f32 v[20:21], v[20:21], v[162:163], v[80:81] op_sel_hi:[1,0,1]
; __device__ __forceinline__ unsigned cvt_pk_bf16(float lo, float hi) { const f32x2_t v = {lo, hi}; const bf16x2_t b = __builtin_convertvector(v, bf16x2_t); return __builtin_bit_cast(unsigned, b); }
;     __device__ __forceinline__ void operator()(const f32x4 (&acc)[2][2][4][2], const Unit& u, int wr, int wc, int fr, int fq, int ui) const {
;     ...
;                 for (int n = 0; n < 2; ++n)
; #pragma unroll
;                     for (int i = 0; i < 4; ++i) { g[n * 4 + i] = fmaf(acc[ai][0][m][n][i], r, bg[n][i]); v[n * 4 + i] = fmaf(acc[ai][1][m][n][i], r, bu[n][i]); }
; #pragma unroll
;                 for (int i = 0; i < 8; ++i) e[i] = __builtin_amdgcn_exp2f(g[i] * (-LOG2E));
; #pragma unroll
;                 for (int i = 0; i < 8; ++i) e[i] = __builtin_amdgcn_rcpf(1.0f + e[i]);
; #pragma unroll
;                 for (int i = 0; i < 8; ++i) e[i] = (g[i] * e[i]) * v[i];
;                 u32x4 w; w.x = cvt_pk_bf16(e[0], e[1]); w.y = cvt_pk_bf16(e[2], e[3]); w.z = cvt_pk_bf16(e[4], e[5]); w.w = cvt_pk_bf16(e[6], e[7]);
;                 *(u32x4*)(act + ((size_t)((row >> 8) * (F / 64) + (jcol >> 6)) * 256 + (row & 255)) * 64 + (jcol & 63)) = w;
	v_pk_mul_f32 v[122:123], v[122:123], v[124:125]
	v_pk_mul_f32 v[124:125], v[116:117], v[222:223] op_sel_hi:[1,0]
	v_exp_f32_e32 v124, v124
	v_exp_f32_e32 v125, v125
	v_pk_fma_f32 v[16:17], v[16:17], v[162:163], v[84:85] op_sel_hi:[1,0,1]
	v_pk_fma_f32 v[18:19], v[18:19], v[162:163], v[86:87] op_sel_hi:[1,0,1]
	v_pk_add_f32 v[124:125], v[124:125], v[224:225] op_sel_hi:[1,0]
	v_rcp_f32_e32 v124, v124
	v_rcp_f32_e32 v125, v125
	s_mov_b32 s65, s67
	v_pk_mul_f32 v[116:117], v[116:117], v[124:125]
	s_nop 0
	v_pk_mul_f32 v[116:117], v[112:113], v[116:117]
	v_pk_fma_f32 v[112:113], v[118:119], v[132:133], v[82:83] op_sel_hi:[1,0,1]
	s_nop 0
	v_pk_mul_f32 v[118:119], v[112:113], v[222:223] op_sel_hi:[1,0]
	v_exp_f32_e32 v118, v118
	v_exp_f32_e32 v119, v119
	s_nop 0
	v_pk_add_f32 v[118:119], v[118:119], v[224:225] op_sel_hi:[1,0]
	v_rcp_f32_e32 v118, v118
	v_rcp_f32_e32 v119, v119
	s_nop 0
	v_pk_mul_f32 v[112:113], v[112:113], v[118:119]
	s_nop 0
	v_pk_mul_f32 v[118:119], v[114:115], v[112:113]
	v_cvt_pk_bf16_f32 v112, v120, v121
	v_cvt_pk_bf16_f32 v113, v122, v123
	v_cvt_pk_bf16_f32 v114, v116, v117
	v_cvt_pk_bf16_f32 v115, v118, v119
	global_store_dwordx4 v[130:131], v[112:115], off offset:2048
	s_nop 1
	v_pk_mul_f32 v[112:113], v[108:109], v[222:223] op_sel_hi:[1,0]
	v_exp_f32_e32 v112, v112
	v_exp_f32_e32 v113, v113
	s_nop 0
	v_pk_add_f32 v[112:113], v[112:113], v[224:225] op_sel_hi:[1,0]
	v_rcp_f32_e32 v112, v112
	v_rcp_f32_e32 v113, v113
	s_nop 0
	v_pk_mul_f32 v[108:109], v[108:109], v[112:113]
	s_nop 0
	v_pk_mul_f32 v[104:105], v[104:105], v[108:109]
	v_pk_fma_f32 v[108:109], v[110:111], v[176:177], v[98:99] op_sel_hi:[1,0,1]
	s_nop 0
	v_pk_mul_f32 v[110:111], v[108:109], v[222:223] op_sel_hi:[1,0]
	v_exp_f32_e32 v110, v110
	v_exp_f32_e32 v111, v111
	s_nop 0
	v_pk_add_f32 v[110:111], v[110:111], v[224:225] op_sel_hi:[1,0]
	v_rcp_f32_e32 v110, v110
	v_rcp_f32_e32 v111, v111
	s_nop 0
	v_pk_mul_f32 v[108:109], v[108:109], v[110:111]
	s_nop 0
	v_pk_mul_f32 v[106:107], v[106:107], v[108:109]
	v_pk_mul_f32 v[108:109], v[92:93], v[222:223] op_sel_hi:[1,0]
	v_exp_f32_e32 v108, v108
	v_exp_f32_e32 v109, v109
	s_nop 0
	v_pk_add_f32 v[108:109], v[108:109], v[224:225] op_sel_hi:[1,0]
	v_rcp_f32_e32 v108, v108
	v_rcp_f32_e32 v109, v109
	s_nop 0
	v_pk_mul_f32 v[92:93], v[92:93], v[108:109]
	s_nop 0
	v_pk_mul_f32 v[92:93], v[88:89], v[92:93]
	v_pk_fma_f32 v[88:89], v[94:95], v[176:177], v[82:83] op_sel_hi:[1,0,1]
	s_nop 0
	v_pk_mul_f32 v[94:95], v[88:89], v[222:223] op_sel_hi:[1,0]
	v_exp_f32_e32 v94, v94
	v_exp_f32_e32 v95, v95
	s_nop 0
	v_pk_add_f32 v[94:95], v[94:95], v[224:225] op_sel_hi:[1,0]
	v_rcp_f32_e32 v94, v94
	v_rcp_f32_e32 v95, v95
	s_nop 0
	v_pk_mul_f32 v[88:89], v[88:89], v[94:95]
	s_nop 0
	v_pk_mul_f32 v[94:95], v[90:91], v[88:89]
	v_cvt_pk_bf16_f32 v90, v92, v93
	v_add_co_u32_e32 v92, vcc, s18, v130
	v_cvt_pk_bf16_f32 v88, v104, v105
	v_cvt_pk_bf16_f32 v89, v106, v107
	v_cvt_pk_bf16_f32 v91, v94, v95
	v_addc_co_u32_e32 v93, vcc, 0, v131, vcc
	global_store_dwordx4 v[92:93], v[88:91], off
	s_nop 1
	v_mov_b32_e32 v88, v177
	v_pk_fma_f32 v[76:77], v[76:77], v[88:89], v[96:97] op_sel_hi:[1,0,1]
	v_pk_fma_f32 v[72:73], v[72:73], v[88:89], v[100:101] op_sel_hi:[1,0,1]
	v_mul_f32_e32 v89, 0xbfb8aa3b, v76
	v_exp_f32_e32 v89, v89
	v_mul_f32_e32 v90, 0xbfb8aa3b, v77
	v_exp_f32_e32 v91, v90
	v_add_f32_e32 v89, 1.0, v89
	v_rcp_f32_e32 v90, v89
	v_add_f32_e32 v89, 1.0, v91
	v_rcp_f32_e32 v91, v89
	v_pk_fma_f32 v[74:75], v[74:75], v[88:89], v[102:103] op_sel_hi:[1,0,1]
	v_pk_fma_f32 v[68:69], v[68:69], v[88:89], v[80:81] op_sel_hi:[1,0,1]
	v_pk_fma_f32 v[64:65], v[64:65], v[88:89], v[84:85] op_sel_hi:[1,0,1]
	v_pk_mul_f32 v[76:77], v[76:77], v[90:91]
	v_pk_fma_f32 v[66:67], v[66:67], v[88:89], v[86:87] op_sel_hi:[1,0,1]
	v_pk_mul_f32 v[72:73], v[72:73], v[76:77]
	v_pk_fma_f32 v[76:77], v[78:79], v[88:89], v[98:99] op_sel_hi:[1,0,1]
	s_nop 0
	v_pk_mul_f32 v[78:79], v[76:77], v[222:223] op_sel_hi:[1,0]
	v_exp_f32_e32 v78, v78
	v_exp_f32_e32 v79, v79
	s_nop 0
	v_pk_add_f32 v[78:79], v[78:79], v[224:225] op_sel_hi:[1,0]
	v_rcp_f32_e32 v78, v78
	v_rcp_f32_e32 v79, v79
	s_nop 0
	v_pk_mul_f32 v[76:77], v[76:77], v[78:79]
	s_nop 0
	v_pk_mul_f32 v[74:75], v[74:75], v[76:77]
	v_pk_mul_f32 v[76:77], v[68:69], v[222:223] op_sel_hi:[1,0]
	v_exp_f32_e32 v76, v76
	v_exp_f32_e32 v77, v77
	s_nop 0
	v_pk_add_f32 v[76:77], v[76:77], v[224:225] op_sel_hi:[1,0]
	v_rcp_f32_e32 v76, v76
	v_rcp_f32_e32 v77, v77
	s_nop 0
	v_pk_mul_f32 v[68:69], v[68:69], v[76:77]
	s_nop 0
	v_pk_mul_f32 v[68:69], v[64:65], v[68:69]
	v_pk_fma_f32 v[64:65], v[70:71], v[88:89], v[82:83] op_sel_hi:[1,0,1]
	s_nop 0
	v_pk_mul_f32 v[70:71], v[64:65], v[222:223] op_sel_hi:[1,0]
	v_exp_f32_e32 v70, v70
	v_exp_f32_e32 v71, v71
	s_nop 0
	v_pk_add_f32 v[70:71], v[70:71], v[224:225] op_sel_hi:[1,0]
	v_rcp_f32_e32 v70, v70
	v_rcp_f32_e32 v71, v71
	s_nop 0
	v_pk_mul_f32 v[64:65], v[64:65], v[70:71]
	s_nop 0
	v_pk_mul_f32 v[70:71], v[66:67], v[64:65]
	v_cvt_pk_bf16_f32 v64, v72, v73
	v_cvt_pk_bf16_f32 v65, v74, v75
	v_cvt_pk_bf16_f32 v66, v68, v69
	v_cvt_pk_bf16_f32 v67, v70, v71
	global_store_dwordx4 v[92:93], v[64:67], off offset:2048
	s_nop 1
	v_pk_mul_f32 v[64:65], v[60:61], v[222:223] op_sel_hi:[1,0]
	v_exp_f32_e32 v64, v64
	v_exp_f32_e32 v65, v65
	s_nop 0
	v_pk_add_f32 v[64:65], v[64:65], v[224:225] op_sel_hi:[1,0]
	v_rcp_f32_e32 v64, v64
	v_rcp_f32_e32 v65, v65
	s_nop 0
	v_pk_mul_f32 v[60:61], v[60:61], v[64:65]
	s_nop 0
	v_pk_mul_f32 v[56:57], v[56:57], v[60:61]
	v_pk_fma_f32 v[60:61], v[62:63], v[164:165], v[98:99] op_sel_hi:[1,0,1]
	s_nop 0
	v_pk_mul_f32 v[62:63], v[60:61], v[222:223] op_sel_hi:[1,0]
; __device__ __forceinline__ unsigned cvt_pk_bf16(float lo, float hi) { const f32x2_t v = {lo, hi}; const bf16x2_t b = __builtin_convertvector(v, bf16x2_t); return __builtin_bit_cast(unsigned, b); }
;     __device__ __forceinline__ void operator()(const f32x4 (&acc)[2][2][4][2], const Unit& u, int wr, int wc, int fr, int fq, int ui) const {
;     ...
;                 for (int n = 0; n < 2; ++n)
; #pragma unroll
;                     for (int i = 0; i < 4; ++i) { g[n * 4 + i] = fmaf(acc[ai][0][m][n][i], r, bg[n][i]); v[n * 4 + i] = fmaf(acc[ai][1][m][n][i], r, bu[n][i]); }
; #pragma unroll
;                 for (int i = 0; i < 8; ++i) e[i] = __builtin_amdgcn_exp2f(g[i] * (-LOG2E));
; #pragma unroll
;                 for (int i = 0; i < 8; ++i) e[i] = __builtin_amdgcn_rcpf(1.0f + e[i]);
; #pragma unroll
;                 for (int i = 0; i < 8; ++i) e[i] = (g[i] * e[i]) * v[i];
;                 u32x4 w; w.x = cvt_pk_bf16(e[0], e[1]); w.y = cvt_pk_bf16(e[2], e[3]); w.z = cvt_pk_bf16(e[4], e[5]); w.w = cvt_pk_bf16(e[6], e[7]);
;                 *(u32x4*)(act + ((size_t)((row >> 8) * (F / 64) + (jcol >> 6)) * 256 + (row & 255)) * 64 + (jcol & 63)) = w;
	v_exp_f32_e32 v62, v62
	v_exp_f32_e32 v63, v63
	s_nop 0
	v_pk_add_f32 v[62:63], v[62:63], v[224:225] op_sel_hi:[1,0]
	v_rcp_f32_e32 v62, v62
	v_rcp_f32_e32 v63, v63
	s_nop 0
	v_pk_mul_f32 v[60:61], v[60:61], v[62:63]
	s_nop 0
	v_pk_mul_f32 v[58:59], v[58:59], v[60:61]
	v_pk_mul_f32 v[60:61], v[52:53], v[222:223] op_sel_hi:[1,0]
	v_exp_f32_e32 v60, v60
	v_exp_f32_e32 v61, v61
	s_nop 0
	v_pk_add_f32 v[60:61], v[60:61], v[224:225] op_sel_hi:[1,0]
	v_rcp_f32_e32 v60, v60
	v_rcp_f32_e32 v61, v61
	s_nop 0
	v_pk_mul_f32 v[52:53], v[52:53], v[60:61]
	s_nop 0
	v_pk_mul_f32 v[48:49], v[48:49], v[52:53]
	v_pk_fma_f32 v[52:53], v[54:55], v[164:165], v[82:83] op_sel_hi:[1,0,1]
	s_nop 0
	v_pk_mul_f32 v[54:55], v[52:53], v[222:223] op_sel_hi:[1,0]
	v_exp_f32_e32 v54, v54
	v_exp_f32_e32 v55, v55
	s_nop 0
	v_pk_add_f32 v[54:55], v[54:55], v[224:225] op_sel_hi:[1,0]
	v_rcp_f32_e32 v54, v54
	v_rcp_f32_e32 v55, v55
	s_nop 0
	v_pk_mul_f32 v[52:53], v[52:53], v[54:55]
	s_nop 0
	v_pk_mul_f32 v[54:55], v[50:51], v[52:53]
	v_cvt_pk_bf16_f32 v52, v48, v49
	v_lshl_add_u64 v[48:49], v[156:157], 0, s[16:17]
	v_cvt_pk_bf16_f32 v50, v56, v57
	v_cvt_pk_bf16_f32 v51, v58, v59
	v_cvt_pk_bf16_f32 v53, v54, v55
	v_lshl_add_u64 v[48:49], v[48:49], 0, v[128:129]
	global_store_dwordx4 v[48:49], v[50:53], off
	s_mov_b64 s[16:17], -1
	s_nop 0
	v_mov_b32_e32 v50, v165
	v_pk_fma_f32 v[44:45], v[44:45], v[50:51], v[96:97] op_sel_hi:[1,0,1]
	v_pk_fma_f32 v[40:41], v[40:41], v[50:51], v[100:101] op_sel_hi:[1,0,1]
	v_mul_f32_e32 v51, 0xbfb8aa3b, v44
	v_exp_f32_e32 v51, v51
	v_mul_f32_e32 v52, 0xbfb8aa3b, v45
	v_exp_f32_e32 v53, v52
	v_add_f32_e32 v51, 1.0, v51
	v_rcp_f32_e32 v52, v51
	v_add_f32_e32 v51, 1.0, v53
	v_rcp_f32_e32 v53, v51
	v_pk_fma_f32 v[42:43], v[42:43], v[50:51], v[102:103] op_sel_hi:[1,0,1]
	v_pk_fma_f32 v[36:37], v[36:37], v[50:51], v[80:81] op_sel_hi:[1,0,1]
	v_pk_fma_f32 v[32:33], v[32:33], v[50:51], v[84:85] op_sel_hi:[1,0,1]
	v_pk_mul_f32 v[44:45], v[44:45], v[52:53]
	v_pk_fma_f32 v[34:35], v[34:35], v[50:51], v[86:87] op_sel_hi:[1,0,1]
	v_pk_mul_f32 v[40:41], v[40:41], v[44:45]
	v_pk_fma_f32 v[44:45], v[46:47], v[50:51], v[98:99] op_sel_hi:[1,0,1]
	s_nop 0
	v_pk_mul_f32 v[46:47], v[44:45], v[222:223] op_sel_hi:[1,0]
	v_exp_f32_e32 v46, v46
	v_exp_f32_e32 v47, v47
	s_nop 0
	v_pk_add_f32 v[46:47], v[46:47], v[224:225] op_sel_hi:[1,0]
	v_rcp_f32_e32 v46, v46
	v_rcp_f32_e32 v47, v47
	s_nop 0
	v_pk_mul_f32 v[44:45], v[44:45], v[46:47]
	s_nop 0
	v_pk_mul_f32 v[42:43], v[42:43], v[44:45]
	v_pk_mul_f32 v[44:45], v[36:37], v[222:223] op_sel_hi:[1,0]
	v_exp_f32_e32 v44, v44
	v_exp_f32_e32 v45, v45
	s_nop 0
	v_pk_add_f32 v[44:45], v[44:45], v[224:225] op_sel_hi:[1,0]
	v_rcp_f32_e32 v44, v44
	v_rcp_f32_e32 v45, v45
	s_nop 0
	v_pk_mul_f32 v[36:37], v[36:37], v[44:45]
	s_nop 0
	v_pk_mul_f32 v[36:37], v[32:33], v[36:37]
	v_pk_fma_f32 v[32:33], v[38:39], v[50:51], v[82:83] op_sel_hi:[1,0,1]
	s_nop 0
	v_pk_mul_f32 v[38:39], v[32:33], v[222:223] op_sel_hi:[1,0]
	v_exp_f32_e32 v38, v38
	v_exp_f32_e32 v39, v39
	s_nop 0
	v_pk_add_f32 v[38:39], v[38:39], v[224:225] op_sel_hi:[1,0]
	v_rcp_f32_e32 v38, v38
	v_rcp_f32_e32 v39, v39
	s_nop 0
	v_pk_mul_f32 v[32:33], v[32:33], v[38:39]
	s_nop 0
	v_pk_mul_f32 v[38:39], v[34:35], v[32:33]
	v_cvt_pk_bf16_f32 v32, v40, v41
	v_cvt_pk_bf16_f32 v33, v42, v43
	v_cvt_pk_bf16_f32 v34, v36, v37
	v_cvt_pk_bf16_f32 v35, v38, v39
	global_store_dwordx4 v[48:49], v[32:35], off offset:2048
	s_nop 1
	v_pk_mul_f32 v[32:33], v[28:29], v[222:223] op_sel_hi:[1,0]
	v_exp_f32_e32 v32, v32
	v_exp_f32_e32 v33, v33
	s_nop 0
	v_pk_add_f32 v[32:33], v[32:33], v[224:225] op_sel_hi:[1,0]
	v_rcp_f32_e32 v32, v32
	v_rcp_f32_e32 v33, v33
	s_nop 0
; __device__ __forceinline__ unsigned cvt_pk_bf16(float lo, float hi) { const f32x2_t v = {lo, hi}; const bf16x2_t b = __builtin_convertvector(v, bf16x2_t); return __builtin_bit_cast(unsigned, b); }
; #define PG8_BAR __builtin_amdgcn_s_barrier()
;     __device__ __forceinline__ void operator()(const f32x4 (&acc)[2][2][4][2], const Unit& u, int wr, int wc, int fr, int fq, int ui) const {
;     ...
;                 for (int n = 0; n < 2; ++n)
; #pragma unroll
;                     for (int i = 0; i < 4; ++i) { g[n * 4 + i] = fmaf(acc[ai][0][m][n][i], r, bg[n][i]); v[n * 4 + i] = fmaf(acc[ai][1][m][n][i], r, bu[n][i]); }
; #pragma unroll
;                 for (int i = 0; i < 8; ++i) e[i] = __builtin_amdgcn_exp2f(g[i] * (-LOG2E));
; #pragma unroll
;                 for (int i = 0; i < 8; ++i) e[i] = __builtin_amdgcn_rcpf(1.0f + e[i]);
; #pragma unroll
;                 for (int i = 0; i < 8; ++i) e[i] = (g[i] * e[i]) * v[i];
;                 u32x4 w; w.x = cvt_pk_bf16(e[0], e[1]); w.y = cvt_pk_bf16(e[2], e[3]); w.z = cvt_pk_bf16(e[4], e[5]); w.w = cvt_pk_bf16(e[6], e[7]);
;                 *(u32x4*)(act + ((size_t)((row >> 8) * (F / 64) + (jcol >> 6)) * 256 + (row & 255)) * 64 + (jcol & 63)) = w;
; template <class Epi, class Sched, bool ALIGN_EPI>
; __device__ __forceinline__ void gemm_phase(PG8_LAS unsigned char* lds, const Gemm g, const Sched& S, const Epi& E, const int tid) {
;     ...
;         }
;         if constexpr (ALIGN_EPI) { if (wr == 0) PG8_BAR; }
;         E(acc, cur, wr, wc, fr, fq, ui); S.done(cur);
;         if (!has_next) break;
; #pragma unroll
;         for (int a = 0; a < 2; ++a)
; #pragma unroll
;             for (int b = 0; b < 2; ++b)
; #pragma unroll
;                 for (int m = 0; m < 4; ++m)
; #pragma unroll
;                     for (int n = 0; n < 2; ++n) acc[a][b][m][n] = (f32x4){0.f, 0.f, 0.f, 0.f};
;         cur = nxt; cA = nA; cB = nB; ++ui;
;         if constexpr (ALIGN_EPI) { if (wr == 1) PG8_BAR; }
	v_pk_mul_f32 v[28:29], v[28:29], v[32:33]
	s_nop 0
	v_pk_mul_f32 v[24:25], v[24:25], v[28:29]
	v_pk_fma_f32 v[28:29], v[30:31], v[162:163], v[98:99] op_sel_hi:[1,0,1]
	s_nop 0
	v_pk_mul_f32 v[30:31], v[28:29], v[222:223] op_sel_hi:[1,0]
	v_exp_f32_e32 v30, v30
	v_exp_f32_e32 v31, v31
	s_nop 0
	v_pk_add_f32 v[30:31], v[30:31], v[224:225] op_sel_hi:[1,0]
	v_rcp_f32_e32 v30, v30
	v_rcp_f32_e32 v31, v31
	s_nop 0
	v_pk_mul_f32 v[28:29], v[28:29], v[30:31]
	s_nop 0
	v_pk_mul_f32 v[26:27], v[26:27], v[28:29]
	v_pk_mul_f32 v[28:29], v[20:21], v[222:223] op_sel_hi:[1,0]
	v_exp_f32_e32 v28, v28
	v_exp_f32_e32 v29, v29
	s_nop 0
	v_pk_add_f32 v[28:29], v[28:29], v[224:225] op_sel_hi:[1,0]
	v_rcp_f32_e32 v28, v28
	v_rcp_f32_e32 v29, v29
	s_nop 0
	v_pk_mul_f32 v[20:21], v[20:21], v[28:29]
	s_nop 0
	v_pk_mul_f32 v[20:21], v[16:17], v[20:21]
	v_pk_fma_f32 v[16:17], v[22:23], v[162:163], v[82:83] op_sel_hi:[1,0,1]
	s_nop 0
	v_pk_mul_f32 v[22:23], v[16:17], v[222:223] op_sel_hi:[1,0]
	v_exp_f32_e32 v22, v22
	v_exp_f32_e32 v23, v23
	s_nop 0
	v_pk_add_f32 v[22:23], v[22:23], v[224:225] op_sel_hi:[1,0]
	v_rcp_f32_e32 v22, v22
	v_rcp_f32_e32 v23, v23
	s_nop 0
	v_pk_mul_f32 v[16:17], v[16:17], v[22:23]
	s_nop 0
	v_pk_mul_f32 v[22:23], v[18:19], v[16:17]
	v_cvt_pk_bf16_f32 v18, v20, v21
	v_add_co_u32_e32 v20, vcc, s18, v48
	v_cvt_pk_bf16_f32 v16, v24, v25
	v_cvt_pk_bf16_f32 v17, v26, v27
	v_cvt_pk_bf16_f32 v19, v22, v23
	v_addc_co_u32_e32 v21, vcc, 0, v49, vcc
	global_store_dwordx4 v[20:21], v[16:19], off
	s_andn2_b64 vcc, exec, s[2:3]
	s_nop 0
	v_mov_b32_e32 v16, v163
	v_pk_fma_f32 v[12:13], v[12:13], v[16:17], v[96:97] op_sel_hi:[1,0,1]
	v_pk_fma_f32 v[8:9], v[8:9], v[16:17], v[100:101] op_sel_hi:[1,0,1]
	v_mul_f32_e32 v17, 0xbfb8aa3b, v12
	v_exp_f32_e32 v17, v17
	v_mul_f32_e32 v18, 0xbfb8aa3b, v13
	v_exp_f32_e32 v19, v18
	v_add_f32_e32 v17, 1.0, v17
	v_rcp_f32_e32 v18, v17
	v_add_f32_e32 v17, 1.0, v19
	v_rcp_f32_e32 v19, v17
	v_pk_fma_f32 v[10:11], v[10:11], v[16:17], v[102:103] op_sel_hi:[1,0,1]
	v_pk_fma_f32 v[4:5], v[4:5], v[16:17], v[80:81] op_sel_hi:[1,0,1]
	v_pk_fma_f32 v[0:1], v[0:1], v[16:17], v[84:85] op_sel_hi:[1,0,1]
	v_pk_mul_f32 v[12:13], v[12:13], v[18:19]
	v_pk_fma_f32 v[2:3], v[2:3], v[16:17], v[86:87] op_sel_hi:[1,0,1]
	v_pk_mul_f32 v[8:9], v[8:9], v[12:13]
	v_pk_fma_f32 v[12:13], v[14:15], v[16:17], v[98:99] op_sel_hi:[1,0,1]
	s_nop 0
	v_pk_mul_f32 v[14:15], v[12:13], v[222:223] op_sel_hi:[1,0]
	v_exp_f32_e32 v14, v14
	v_exp_f32_e32 v15, v15
	s_nop 0
	v_pk_add_f32 v[14:15], v[14:15], v[224:225] op_sel_hi:[1,0]
	v_rcp_f32_e32 v14, v14
	v_rcp_f32_e32 v15, v15
	s_nop 0
	v_pk_mul_f32 v[12:13], v[12:13], v[14:15]
	s_nop 0
	v_pk_mul_f32 v[10:11], v[10:11], v[12:13]
	v_pk_mul_f32 v[12:13], v[4:5], v[222:223] op_sel_hi:[1,0]
	v_exp_f32_e32 v12, v12
	v_exp_f32_e32 v13, v13
	s_nop 0
	v_pk_add_f32 v[12:13], v[12:13], v[224:225] op_sel_hi:[1,0]
	v_rcp_f32_e32 v12, v12
	v_rcp_f32_e32 v13, v13
	s_nop 0
	v_pk_mul_f32 v[4:5], v[4:5], v[12:13]
	s_nop 0
	v_pk_mul_f32 v[4:5], v[0:1], v[4:5]
	v_pk_fma_f32 v[0:1], v[6:7], v[16:17], v[82:83] op_sel_hi:[1,0,1]
	s_nop 0
	v_pk_mul_f32 v[6:7], v[0:1], v[222:223] op_sel_hi:[1,0]
	v_exp_f32_e32 v6, v6
	v_exp_f32_e32 v7, v7
	s_nop 0
	v_pk_add_f32 v[6:7], v[6:7], v[224:225] op_sel_hi:[1,0]
	v_rcp_f32_e32 v6, v6
	v_rcp_f32_e32 v7, v7
	s_nop 0
	v_pk_mul_f32 v[0:1], v[0:1], v[6:7]
	s_nop 0
	v_pk_mul_f32 v[6:7], v[2:3], v[0:1]
	v_cvt_pk_bf16_f32 v0, v8, v9
	v_cvt_pk_bf16_f32 v1, v10, v11
	v_cvt_pk_bf16_f32 v2, v4, v5
	v_cvt_pk_bf16_f32 v3, v6, v7
	global_store_dwordx4 v[20:21], v[0:3], off offset:2048
	s_cbranch_vccnz .LBB0_242
	s_andn2_b64 vcc, exec, s[4:5]
	s_cbranch_vccnz .LBB0_241
	s_barrier
	s_branch .LBB0_241
